# phase 0 adaLN GEMV: two k-groups per trip (8 weight loads per lane in flight instead of 4); plus earlier phase-0 / router edits
# baseline (speedup 1.0000x reference)
.LBB0_16:
	s_add_u32 s100, s8, 0x600000
	s_addc_u32 s101, s9, 0
	v_add_u32_e32 v106, 0x200, v36
	v_lshl_add_u64 v[42:43], v[28:29], 0, s[8:9]
	v_lshl_add_u64 v[60:61], v[24:25], 0, s[8:9]
	v_lshl_add_u64 v[62:63], v[22:23], 0, s[8:9]
	v_lshl_add_u64 v[64:65], v[20:21], 0, s[8:9]
	global_load_dwordx4 v[38:41], v[42:43], off nt
	global_load_dwordx4 v[48:51], v[60:61], off nt
	global_load_dwordx4 v[52:55], v[62:63], off nt
	global_load_dwordx4 v[56:59], v[64:65], off nt
	v_lshl_add_u64 v[112:113], v[28:29], 0, s[100:101]
	v_lshl_add_u64 v[130:131], v[24:25], 0, s[100:101]
	v_lshl_add_u64 v[132:133], v[22:23], 0, s[100:101]
	v_lshl_add_u64 v[134:135], v[20:21], 0, s[100:101]
	global_load_dwordx4 v[108:111], v[112:113], off nt
	global_load_dwordx4 v[118:121], v[130:131], off nt
	global_load_dwordx4 v[122:125], v[132:133], off nt
	global_load_dwordx4 v[126:129], v[134:135], off nt
	ds_read2_b32 v[42:43], v36 offset1:32
	v_add_u32_e32 v37, 0x2000, v36
	v_add_u32_e32 v70, 0x4000, v36
	v_add_u32_e32 v72, 0x6000, v36
	ds_read2_b32 v[60:61], v36 offset0:64 offset1:96
	ds_read2_b32 v[62:63], v37 offset1:32
	ds_read2_b32 v[64:65], v70 offset1:32
	ds_read2_b32 v[66:67], v72 offset1:32
	ds_read2_b32 v[68:69], v37 offset0:64 offset1:96
	ds_read2_b32 v[70:71], v70 offset0:64 offset1:96
	ds_read2_b32 v[72:73], v72 offset0:64 offset1:96
	s_waitcnt lgkmcnt(7)
	v_mov_b32_e32 v74, v43
	s_waitcnt lgkmcnt(5)
	v_mov_b32_e32 v78, v63
	s_waitcnt lgkmcnt(4)
	v_mov_b32_e32 v80, v65
	s_waitcnt lgkmcnt(3)
	v_mov_b32_e32 v82, v67
	v_mov_b32_e32 v76, v61
	s_waitcnt lgkmcnt(2)
	v_mov_b32_e32 v84, v69
	s_waitcnt lgkmcnt(1)
	v_mov_b32_e32 v86, v71
	s_waitcnt lgkmcnt(0)
	v_mov_b32_e32 v88, v73
	ds_read2_b32 v[112:113], v106 offset1:32
	v_add_u32_e32 v107, 0x2000, v106
	v_add_u32_e32 v140, 0x4000, v106
	v_add_u32_e32 v142, 0x6000, v106
	ds_read2_b32 v[130:131], v106 offset0:64 offset1:96
	ds_read2_b32 v[132:133], v107 offset1:32
	ds_read2_b32 v[134:135], v140 offset1:32
	ds_read2_b32 v[136:137], v142 offset1:32
	ds_read2_b32 v[138:139], v107 offset0:64 offset1:96
	ds_read2_b32 v[140:141], v140 offset0:64 offset1:96
	ds_read2_b32 v[142:143], v142 offset0:64 offset1:96
	s_waitcnt vmcnt(7)
	v_pk_fma_f32 v[34:35], v[42:43], v[38:39], v[34:35] op_sel_hi:[0,1,1]
	v_pk_fma_f32 v[32:33], v[42:43], v[40:41], v[32:33] op_sel_hi:[0,1,1]
	v_pk_fma_f32 v[30:31], v[38:39], v[62:63], v[30:31] op_sel_hi:[1,0,1]
	v_pk_fma_f32 v[26:27], v[40:41], v[62:63], v[26:27] op_sel_hi:[1,0,1]
	v_pk_fma_f32 v[18:19], v[38:39], v[64:65], v[18:19] op_sel_hi:[1,0,1]
	v_pk_fma_f32 v[16:17], v[40:41], v[64:65], v[16:17] op_sel_hi:[1,0,1]
	v_pk_fma_f32 v[14:15], v[38:39], v[66:67], v[14:15] op_sel_hi:[1,0,1]
	v_pk_fma_f32 v[12:13], v[40:41], v[66:67], v[12:13] op_sel_hi:[1,0,1]
	s_waitcnt vmcnt(6)
	v_pk_fma_f32 v[34:35], v[74:75], v[48:49], v[34:35] op_sel_hi:[0,1,1]
	v_pk_fma_f32 v[32:33], v[74:75], v[50:51], v[32:33] op_sel_hi:[0,1,1]
	v_pk_fma_f32 v[30:31], v[48:49], v[78:79], v[30:31] op_sel_hi:[1,0,1]
	v_pk_fma_f32 v[26:27], v[50:51], v[78:79], v[26:27] op_sel_hi:[1,0,1]
	v_pk_fma_f32 v[18:19], v[48:49], v[80:81], v[18:19] op_sel_hi:[1,0,1]
	v_pk_fma_f32 v[16:17], v[50:51], v[80:81], v[16:17] op_sel_hi:[1,0,1]
	v_pk_fma_f32 v[14:15], v[48:49], v[82:83], v[14:15] op_sel_hi:[1,0,1]
	v_pk_fma_f32 v[12:13], v[50:51], v[82:83], v[12:13] op_sel_hi:[1,0,1]
	s_waitcnt vmcnt(5)
	v_pk_fma_f32 v[34:35], v[60:61], v[52:53], v[34:35] op_sel_hi:[0,1,1]
	v_pk_fma_f32 v[32:33], v[60:61], v[54:55], v[32:33] op_sel_hi:[0,1,1]
	v_pk_fma_f32 v[30:31], v[52:53], v[68:69], v[30:31] op_sel_hi:[1,0,1]
	v_pk_fma_f32 v[26:27], v[54:55], v[68:69], v[26:27] op_sel_hi:[1,0,1]
	v_pk_fma_f32 v[18:19], v[52:53], v[70:71], v[18:19] op_sel_hi:[1,0,1]
	v_pk_fma_f32 v[16:17], v[54:55], v[70:71], v[16:17] op_sel_hi:[1,0,1]
	v_pk_fma_f32 v[14:15], v[52:53], v[72:73], v[14:15] op_sel_hi:[1,0,1]
	v_pk_fma_f32 v[12:13], v[54:55], v[72:73], v[12:13] op_sel_hi:[1,0,1]
	s_waitcnt vmcnt(4)
	v_pk_fma_f32 v[34:35], v[76:77], v[56:57], v[34:35] op_sel_hi:[0,1,1]
	v_pk_fma_f32 v[32:33], v[76:77], v[58:59], v[32:33] op_sel_hi:[0,1,1]
	v_pk_fma_f32 v[30:31], v[56:57], v[84:85], v[30:31] op_sel_hi:[1,0,1]
	v_pk_fma_f32 v[26:27], v[58:59], v[84:85], v[26:27] op_sel_hi:[1,0,1]
	v_pk_fma_f32 v[18:19], v[56:57], v[86:87], v[18:19] op_sel_hi:[1,0,1]
	v_pk_fma_f32 v[16:17], v[58:59], v[86:87], v[16:17] op_sel_hi:[1,0,1]
	v_pk_fma_f32 v[14:15], v[56:57], v[88:89], v[14:15] op_sel_hi:[1,0,1]
	v_pk_fma_f32 v[12:13], v[58:59], v[88:89], v[12:13] op_sel_hi:[1,0,1]
	s_waitcnt lgkmcnt(7)
	v_mov_b32_e32 v144, v113
	s_waitcnt lgkmcnt(5)
	v_mov_b32_e32 v148, v133
	s_waitcnt lgkmcnt(4)
	v_mov_b32_e32 v150, v135
	s_waitcnt lgkmcnt(3)
	v_mov_b32_e32 v152, v137
	v_mov_b32_e32 v146, v131
	s_waitcnt lgkmcnt(2)
	v_mov_b32_e32 v154, v139
	s_waitcnt lgkmcnt(1)
	v_mov_b32_e32 v156, v141
	s_waitcnt lgkmcnt(0)
	v_mov_b32_e32 v158, v143
	s_waitcnt vmcnt(3)
	v_pk_fma_f32 v[34:35], v[112:113], v[108:109], v[34:35] op_sel_hi:[0,1,1]
	v_pk_fma_f32 v[32:33], v[112:113], v[110:111], v[32:33] op_sel_hi:[0,1,1]
	v_pk_fma_f32 v[30:31], v[108:109], v[132:133], v[30:31] op_sel_hi:[1,0,1]
	v_pk_fma_f32 v[26:27], v[110:111], v[132:133], v[26:27] op_sel_hi:[1,0,1]
	v_pk_fma_f32 v[18:19], v[108:109], v[134:135], v[18:19] op_sel_hi:[1,0,1]
	v_pk_fma_f32 v[16:17], v[110:111], v[134:135], v[16:17] op_sel_hi:[1,0,1]
	v_pk_fma_f32 v[14:15], v[108:109], v[136:137], v[14:15] op_sel_hi:[1,0,1]
	v_pk_fma_f32 v[12:13], v[110:111], v[136:137], v[12:13] op_sel_hi:[1,0,1]
	s_waitcnt vmcnt(2)
	v_pk_fma_f32 v[34:35], v[144:145], v[118:119], v[34:35] op_sel_hi:[0,1,1]
	v_pk_fma_f32 v[32:33], v[144:145], v[120:121], v[32:33] op_sel_hi:[0,1,1]
	v_pk_fma_f32 v[30:31], v[118:119], v[148:149], v[30:31] op_sel_hi:[1,0,1]
	v_pk_fma_f32 v[26:27], v[120:121], v[148:149], v[26:27] op_sel_hi:[1,0,1]
	v_pk_fma_f32 v[18:19], v[118:119], v[150:151], v[18:19] op_sel_hi:[1,0,1]
	v_pk_fma_f32 v[16:17], v[120:121], v[150:151], v[16:17] op_sel_hi:[1,0,1]
	v_pk_fma_f32 v[14:15], v[118:119], v[152:153], v[14:15] op_sel_hi:[1,0,1]
	v_pk_fma_f32 v[12:13], v[120:121], v[152:153], v[12:13] op_sel_hi:[1,0,1]
	s_waitcnt vmcnt(1)
	v_pk_fma_f32 v[34:35], v[130:131], v[122:123], v[34:35] op_sel_hi:[0,1,1]
	v_pk_fma_f32 v[32:33], v[130:131], v[124:125], v[32:33] op_sel_hi:[0,1,1]
	v_pk_fma_f32 v[30:31], v[122:123], v[138:139], v[30:31] op_sel_hi:[1,0,1]
	v_pk_fma_f32 v[26:27], v[124:125], v[138:139], v[26:27] op_sel_hi:[1,0,1]
	v_pk_fma_f32 v[18:19], v[122:123], v[140:141], v[18:19] op_sel_hi:[1,0,1]
	v_pk_fma_f32 v[16:17], v[124:125], v[140:141], v[16:17] op_sel_hi:[1,0,1]
	v_pk_fma_f32 v[14:15], v[122:123], v[142:143], v[14:15] op_sel_hi:[1,0,1]
	v_pk_fma_f32 v[12:13], v[124:125], v[142:143], v[12:13] op_sel_hi:[1,0,1]
	s_waitcnt vmcnt(0)
	v_pk_fma_f32 v[34:35], v[146:147], v[126:127], v[34:35] op_sel_hi:[0,1,1]
	v_pk_fma_f32 v[32:33], v[146:147], v[128:129], v[32:33] op_sel_hi:[0,1,1]
	v_pk_fma_f32 v[30:31], v[126:127], v[154:155], v[30:31] op_sel_hi:[1,0,1]
	v_pk_fma_f32 v[26:27], v[128:129], v[154:155], v[26:27] op_sel_hi:[1,0,1]
	v_pk_fma_f32 v[18:19], v[126:127], v[156:157], v[18:19] op_sel_hi:[1,0,1]
	v_pk_fma_f32 v[16:17], v[128:129], v[156:157], v[16:17] op_sel_hi:[1,0,1]
	v_pk_fma_f32 v[14:15], v[126:127], v[158:159], v[14:15] op_sel_hi:[1,0,1]
	v_pk_fma_f32 v[12:13], v[128:129], v[158:159], v[12:13] op_sel_hi:[1,0,1]
	s_add_u32 s8, s8, 0xc00000
	s_addc_u32 s9, s9, 0
	v_add_u32_e32 v36, 0x400, v36
	s_cmp_lg_u32 s8, 0x6000000
	s_cbranch_scc1 .LBB0_16
	ds_bpermute_b32 v20, v0, v34
	ds_bpermute_b32 v21, v0, v35
	ds_bpermute_b32 v24, v0, v32
	ds_bpermute_b32 v25, v0, v33
	ds_bpermute_b32 v36, v0, v18
	ds_bpermute_b32 v37, v0, v19
	s_waitcnt lgkmcnt(4)
	v_pk_add_f32 v[20:21], v[34:35], v[20:21]
	ds_bpermute_b32 v34, v0, v26
	s_waitcnt lgkmcnt(3)
	v_pk_add_f32 v[24:25], v[32:33], v[24:25]
	ds_bpermute_b32 v32, v0, v30
	ds_bpermute_b32 v33, v0, v31
	ds_bpermute_b32 v35, v0, v27
	ds_bpermute_b32 v38, v0, v16
	ds_bpermute_b32 v39, v0, v17
	ds_bpermute_b32 v40, v0, v14
	ds_bpermute_b32 v41, v0, v15
	ds_bpermute_b32 v42, v0, v12
	ds_bpermute_b32 v43, v0, v13
	s_waitcnt lgkmcnt(7)
	v_pk_add_f32 v[30:31], v[30:31], v[32:33]
	s_waitcnt lgkmcnt(6)
	v_pk_add_f32 v[26:27], v[26:27], v[34:35]
	v_pk_add_f32 v[18:19], v[18:19], v[36:37]
	s_waitcnt lgkmcnt(4)
	v_pk_add_f32 v[16:17], v[16:17], v[38:39]
	s_waitcnt lgkmcnt(2)
	v_pk_add_f32 v[14:15], v[14:15], v[40:41]
	s_waitcnt lgkmcnt(0)
	v_pk_add_f32 v[12:13], v[12:13], v[42:43]
	ds_bpermute_b32 v22, v1, v20
	ds_bpermute_b32 v23, v1, v21
	ds_bpermute_b32 v28, v1, v24
	ds_bpermute_b32 v29, v1, v25
	ds_bpermute_b32 v32, v1, v30
	ds_bpermute_b32 v33, v1, v31
	ds_bpermute_b32 v34, v1, v26
	ds_bpermute_b32 v35, v1, v27
	ds_bpermute_b32 v36, v1, v18
	ds_bpermute_b32 v37, v1, v19
	ds_bpermute_b32 v38, v1, v16
	ds_bpermute_b32 v39, v1, v17
	ds_bpermute_b32 v40, v1, v14
	ds_bpermute_b32 v41, v1, v15
	ds_bpermute_b32 v42, v1, v12
	ds_bpermute_b32 v43, v1, v13
	s_and_saveexec_b64 s[8:9], vcc
	s_cbranch_execz .LBB0_19
	s_waitcnt lgkmcnt(14)
	v_pk_add_f32 v[20:21], v[20:21], v[22:23]
	s_waitcnt lgkmcnt(12)
	v_pk_add_f32 v[22:23], v[24:25], v[28:29]
	ds_write_b128 v2, v[20:23] offset:32768
	s_waitcnt lgkmcnt(11)
	v_pk_add_f32 v[20:21], v[30:31], v[32:33]
	s_waitcnt lgkmcnt(9)
	v_pk_add_f32 v[22:23], v[26:27], v[34:35]
	ds_write_b128 v2, v[20:23] offset:32784
	s_waitcnt lgkmcnt(8)
	v_pk_add_f32 v[18:19], v[18:19], v[36:37]
	s_waitcnt lgkmcnt(6)
	v_pk_add_f32 v[20:21], v[16:17], v[38:39]
	s_waitcnt lgkmcnt(4)
	v_pk_add_f32 v[14:15], v[14:15], v[40:41]
	s_waitcnt lgkmcnt(2)
	v_pk_add_f32 v[16:17], v[12:13], v[42:43]
	ds_write_b128 v2, v[18:21] offset:32800
	ds_write_b128 v2, v[14:17] offset:32816
